# split-counter first poll issued together with the arrival atomic; all hand-written polls bounded
# baseline (speedup 1.0000x reference)
.LBB0_143:
	s_lshl_b32 s0, s37, 6
	v_add_u32_e32 v166, s0, v181
	v_ashrrev_i32_e32 v167, 31, v166
	v_lshlrev_b64 v[0:1], 12, v[166:167]
	v_or_b32_e32 v168, 1, v166
	v_lshl_add_u64 v[0:1], v[152:153], 0, v[0:1]
	v_ashrrev_i32_e32 v169, 31, v168
	global_load_dwordx4 v[128:131], v[0:1], off nt
	global_load_dwordx4 v[124:127], v[0:1], off offset:1024 nt
	global_load_dwordx4 v[96:99], v[0:1], off offset:2048 nt
	global_load_dwordx4 v[84:87], v[0:1], off offset:3072 nt
	v_lshlrev_b64 v[0:1], 12, v[168:169]
	v_or_b32_e32 v170, 2, v166
	v_lshl_add_u64 v[0:1], v[152:153], 0, v[0:1]
	v_ashrrev_i32_e32 v171, 31, v170
	global_load_dwordx4 v[132:135], v[0:1], off nt
	global_load_dwordx4 v[112:115], v[0:1], off offset:1024 nt
	global_load_dwordx4 v[100:103], v[0:1], off offset:2048 nt
	global_load_dwordx4 v[88:91], v[0:1], off offset:3072 nt
	v_lshlrev_b64 v[0:1], 12, v[170:171]
	v_or_b32_e32 v172, 3, v166
	v_lshl_add_u64 v[0:1], v[152:153], 0, v[0:1]
	v_ashrrev_i32_e32 v173, 31, v172
	global_load_dwordx4 v[136:139], v[0:1], off nt
	global_load_dwordx4 v[116:119], v[0:1], off offset:1024 nt
	global_load_dwordx4 v[104:107], v[0:1], off offset:2048 nt
	global_load_dwordx4 v[92:95], v[0:1], off offset:3072 nt
	v_lshlrev_b64 v[0:1], 12, v[172:173]
	v_lshl_add_u64 v[0:1], v[152:153], 0, v[0:1]
	global_load_dwordx4 v[140:143], v[0:1], off nt
	global_load_dwordx4 v[120:123], v[0:1], off offset:1024 nt
	global_load_dwordx4 v[108:111], v[0:1], off offset:2048 nt
	global_load_dwordx4 v[80:83], v[0:1], off offset:3072 nt
	v_add_u32_e32 v0, s0, v185
	v_ashrrev_i32_e32 v1, 31, v0
	v_lshlrev_b64 v[2:3], 12, v[0:1]
	v_or_b32_e32 v4, 1, v0
	v_or_b32_e32 v6, 2, v0
	v_or_b32_e32 v0, 3, v0
	s_lshl_b32 s38, s37, 1
	v_ashrrev_i32_e32 v5, 31, v4
	v_ashrrev_i32_e32 v7, 31, v6
	v_ashrrev_i32_e32 v1, 31, v0
	v_or_b32_e32 v8, s38, v188
	v_lshlrev_b64 v[4:5], 12, v[4:5]
	v_lshlrev_b64 v[6:7], 12, v[6:7]
	v_lshlrev_b64 v[0:1], 12, v[0:1]
	v_ashrrev_i32_e32 v9, 31, v8
	v_lshl_add_u64 v[2:3], v[152:153], 0, v[2:3]
	v_lshl_add_u64 v[4:5], v[152:153], 0, v[4:5]
	v_lshl_add_u64 v[6:7], v[152:153], 0, v[6:7]
	v_lshl_add_u64 v[0:1], v[152:153], 0, v[0:1]
	v_lshlrev_b64 v[8:9], 12, v[8:9]
	v_lshl_add_u64 v[144:145], v[154:155], 0, v[8:9]
	global_load_dwordx4 v[76:79], v[2:3], off nt
	global_load_dwordx4 v[60:63], v[2:3], off offset:1024 nt
	global_load_dwordx4 v[44:47], v[2:3], off offset:2048 nt
	global_load_dwordx4 v[20:23], v[2:3], off offset:3072 nt
	global_load_dwordx4 v[72:75], v[4:5], off nt
	global_load_dwordx4 v[56:59], v[4:5], off offset:1024 nt
	global_load_dwordx4 v[40:43], v[4:5], off offset:2048 nt
	global_load_dwordx4 v[24:27], v[4:5], off offset:3072 nt
	global_load_dwordx4 v[68:71], v[6:7], off nt
	global_load_dwordx4 v[52:55], v[6:7], off offset:1024 nt
	global_load_dwordx4 v[36:39], v[6:7], off offset:2048 nt
	global_load_dwordx4 v[28:31], v[6:7], off offset:3072 nt
	global_load_dwordx4 v[64:67], v[0:1], off nt
	global_load_dwordx4 v[48:51], v[0:1], off offset:1024 nt
	global_load_dwordx4 v[32:35], v[0:1], off offset:2048 nt
	global_load_dwordx4 v[16:19], v[0:1], off offset:3072 nt
	global_load_dwordx4 v[12:15], v[144:145], off
	global_load_dwordx4 v[8:11], v[144:145], off offset:1024
	global_load_dwordx4 v[4:7], v[144:145], off offset:2048
	s_nop 0
	global_load_dwordx4 v[0:3], v[144:145], off offset:3072
	s_waitcnt vmcnt(63) expcnt(7) lgkmcnt(15)
	v_readfirstlane_b32 s100, v186
	s_nop 0
	s_cmp_lg_u32 s100, 0
	s_cbranch_scc1 .Lada_wait_skip
	v_readlane_b32 s100, v235, 7
	v_readlane_b32 s101, v235, 8
	v_mov_b32_e32 v236, 0x80
	v_mov_b32_e32 v239, 0
	s_nop 3
.Lada_poll:
	global_load_dword v237, v236, s[100:101] sc1
	s_waitcnt vmcnt(0)
	v_readfirstlane_b32 s99, v237
	s_nop 0
	s_cmp_ge_u32 s99, 0xc0
	s_cbranch_scc1 .Lada_wait_skip
	s_sleep 1
	v_add_u32_e32 v239, 1, v239
	v_readfirstlane_b32 s99, v239
	s_nop 0
	s_cmp_lt_u32 s99, 0x8000
	s_cbranch_scc1 .Lada_poll

.LBB0_389:
	s_mov_b64 s[8:9], exec
	v_readlane_b32 s2, v235, 9
	s_lshl_b32 s2, s2, 8
	v_readlane_b32 s10, v235, 7
	v_mbcnt_lo_u32_b32 v1, s8, 0
	v_readlane_b32 s11, v235, 8
	s_add_u32 s2, s10, s2
	v_mbcnt_hi_u32_b32 v1, s9, v1
	s_addc_u32 s3, s11, 0
	v_cmp_eq_u32_e32 vcc, 0, v1
	s_and_saveexec_b64 s[10:11], vcc
	s_cbranch_execz .LBB0_391
	s_bcnt1_i32_b64 s8, s[8:9]
	v_mov_b32_e32 v3, 0x1000
	v_mov_b32_e32 v4, s8
	global_atomic_add v3, v3, v4, s[2:3] offset:1024 sc0
	buffer_inv sc1
	v_readlane_b32 s100, v235, 7
	v_readlane_b32 s101, v235, 8
	v_mov_b32_e32 v241, 0x2c00
	s_nop 3
	global_load_dword v240, v241, s[100:101] sc1

.Lxb_poll_3:
	v_readfirstlane_b32 s98, v236
	v_mov_b32_e32 v237, 0x2c00
	v_mov_b32_e32 v239, 0
	s_waitcnt vmcnt(0)
	v_cmp_ge_u32_e32 vcc, v240, v0
	s_cbranch_vccnz .Lxb_done_3

.LBB0_516:
	s_mov_b64 s[6:7], exec
	v_readlane_b32 s2, v235, 9
	s_lshl_b32 s2, s2, 8
	v_readlane_b32 s8, v235, 7
	v_mbcnt_lo_u32_b32 v1, s6, 0
	v_readlane_b32 s9, v235, 8
	s_add_u32 s2, s8, s2
	v_mbcnt_hi_u32_b32 v1, s7, v1
	s_addc_u32 s3, s9, 0
	v_cmp_eq_u32_e32 vcc, 0, v1
	s_and_saveexec_b64 s[8:9], vcc
	s_cbranch_execz .LBB0_518
	s_bcnt1_i32_b64 s6, s[6:7]
	v_mov_b32_e32 v3, 0x1000
	v_mov_b32_e32 v4, s6
	global_atomic_add v3, v3, v4, s[2:3] offset:1024 sc0
	buffer_inv sc1
	v_readlane_b32 s100, v235, 7
	v_readlane_b32 s101, v235, 8
	v_mov_b32_e32 v241, 0x2c80
	s_nop 3
	global_load_dword v240, v241, s[100:101] sc1

.Lxb_poll_5:
	v_readfirstlane_b32 s98, v236
	v_mov_b32_e32 v237, 0x2c80
	v_mov_b32_e32 v239, 0
	s_waitcnt vmcnt(0)
	v_cmp_ge_u32_e32 vcc, v240, v0
	s_cbranch_vccnz .Lxb_done_5

.LBB0_650:
	s_or_b64 exec, exec, s[0:1]
	v_readfirstlane_b32 s100, v186
	s_nop 0
	s_cmp_lg_u32 s100, 0
	s_cbranch_scc1 .Lp7_w_skip
	s_cmp_eq_u32 s98, 0
	s_cbranch_scc1 .Lp7_w_skip
	v_readlane_b32 s100, v235, 7
	v_readlane_b32 s101, v235, 8
	v_mov_b32_e32 v236, 0x3400
	v_mov_b32_e32 v239, 0
	s_nop 3
